# speedup vs baseline: 1.0048x; 1.0048x over previous
.LBB4_52:
	v_mov_b32_e32 v18, v42
	v_mov_b32_e32 v22, v41
	ds_read_b128 v[2:5], v0
	ds_read_b128 v[6:9], v0 offset:16
	ds_read2_b32 v[10:11], v18 offset1:100
	ds_read2_b32 v[24:25], v22 offset1:100
	v_add_u32_e32 v19, 0x200, v18
	v_add_u32_e32 v23, 0x200, v22
	ds_read2_b32 v[12:13], v19 offset0:72 offset1:172
	ds_read2_b32 v[26:27], v23 offset0:72 offset1:172
	v_add_u32_e32 v20, 0x400, v18
	v_add_u32_e32 v32, 0x400, v22
	ds_read2_b32 v[14:15], v20 offset0:144 offset1:244
	ds_read2_b32 v[28:29], v32 offset0:144 offset1:244
	v_add_u32_e32 v21, 0x800, v18
	v_add_u32_e32 v33, 0x800, v22
	ds_read2_b32 v[16:17], v21 offset0:88 offset1:188
	ds_read2_b32 v[30:31], v33 offset0:88 offset1:188
	v_add_u32_e32 v70, 0xc80, v42
	v_add_u32_e32 v74, 0xc80, v41
	ds_read_b128 v[46:49], v0 offset:32
	ds_read_b128 v[50:53], v0 offset:48
	ds_read2_b32 v[54:55], v70 offset1:100
	ds_read2_b32 v[62:63], v74 offset1:100
	v_add_u32_e32 v71, 0x200, v70
	v_add_u32_e32 v75, 0x200, v74
	ds_read2_b32 v[56:57], v71 offset0:72 offset1:172
	ds_read2_b32 v[64:65], v75 offset0:72 offset1:172
	v_add_u32_e32 v72, 0x400, v70
	v_add_u32_e32 v76, 0x400, v74
	ds_read2_b32 v[58:59], v72 offset0:144 offset1:244
	ds_read2_b32 v[66:67], v76 offset0:144 offset1:244
	v_add_u32_e32 v73, 0x800, v70
	v_add_u32_e32 v77, 0x800, v74
	ds_read2_b32 v[60:61], v73 offset0:88 offset1:188
	ds_read2_b32 v[68:69], v77 offset0:88 offset1:188
	s_waitcnt lgkmcnt(10)
	v_fmac_f32_e32 v39, v2, v10
	v_fmac_f32_e32 v38, v2, v24
	v_fmac_f32_e32 v39, v3, v11
	v_fmac_f32_e32 v38, v3, v25
	v_fmac_f32_e32 v39, v4, v12
	v_fmac_f32_e32 v38, v4, v26
	v_fmac_f32_e32 v39, v5, v13
	v_fmac_f32_e32 v38, v5, v27
	v_fmac_f32_e32 v39, v6, v14
	v_fmac_f32_e32 v38, v6, v28
	v_fmac_f32_e32 v39, v7, v15
	v_fmac_f32_e32 v38, v7, v29
	v_fmac_f32_e32 v39, v8, v16
	v_fmac_f32_e32 v38, v8, v30
	v_fmac_f32_e32 v39, v9, v17
	v_fmac_f32_e32 v38, v9, v31
	v_add_u32_e32 v18, 0x1900, v42
	v_add_u32_e32 v22, 0x1900, v41
	ds_read_b128 v[2:5], v0 offset:64
	ds_read_b128 v[6:9], v0 offset:80
	ds_read2_b32 v[10:11], v18 offset1:100
	ds_read2_b32 v[24:25], v22 offset1:100
	v_add_u32_e32 v19, 0x200, v18
	v_add_u32_e32 v23, 0x200, v22
	ds_read2_b32 v[12:13], v19 offset0:72 offset1:172
	ds_read2_b32 v[26:27], v23 offset0:72 offset1:172
	v_add_u32_e32 v20, 0x400, v18
	v_add_u32_e32 v32, 0x400, v22
	ds_read2_b32 v[14:15], v20 offset0:144 offset1:244
	ds_read2_b32 v[28:29], v32 offset0:144 offset1:244
	v_add_u32_e32 v21, 0x800, v18
	v_add_u32_e32 v33, 0x800, v22
	ds_read2_b32 v[16:17], v21 offset0:88 offset1:188
	ds_read2_b32 v[30:31], v33 offset0:88 offset1:188
	s_waitcnt lgkmcnt(10)
	v_fmac_f32_e32 v39, v46, v54
	v_fmac_f32_e32 v38, v46, v62
	v_fmac_f32_e32 v39, v47, v55
	v_fmac_f32_e32 v38, v47, v63
	v_fmac_f32_e32 v39, v48, v56
	v_fmac_f32_e32 v38, v48, v64
	v_fmac_f32_e32 v39, v49, v57
	v_fmac_f32_e32 v38, v49, v65
	v_fmac_f32_e32 v39, v50, v58
	v_fmac_f32_e32 v38, v50, v66
	v_fmac_f32_e32 v39, v51, v59
	v_fmac_f32_e32 v38, v51, v67
	v_fmac_f32_e32 v39, v52, v60
	v_fmac_f32_e32 v38, v52, v68
	v_fmac_f32_e32 v39, v53, v61
	v_fmac_f32_e32 v38, v53, v69
	v_add_u32_e32 v70, 0x2580, v42
	v_add_u32_e32 v74, 0x2580, v41
	ds_read_b128 v[46:49], v0 offset:96
	ds_read_b128 v[50:53], v0 offset:112
	ds_read2_b32 v[54:55], v70 offset1:100
	ds_read2_b32 v[62:63], v74 offset1:100
	v_add_u32_e32 v71, 0x200, v70
	v_add_u32_e32 v75, 0x200, v74
	ds_read2_b32 v[56:57], v71 offset0:72 offset1:172
	ds_read2_b32 v[64:65], v75 offset0:72 offset1:172
	v_add_u32_e32 v72, 0x400, v70
	v_add_u32_e32 v76, 0x400, v74
	ds_read2_b32 v[58:59], v72 offset0:144 offset1:244
	ds_read2_b32 v[66:67], v76 offset0:144 offset1:244
	v_add_u32_e32 v73, 0x800, v70
	v_add_u32_e32 v77, 0x800, v74
	ds_read2_b32 v[60:61], v73 offset0:88 offset1:188
	ds_read2_b32 v[68:69], v77 offset0:88 offset1:188
	s_waitcnt lgkmcnt(10)
	v_fmac_f32_e32 v39, v2, v10
	v_fmac_f32_e32 v38, v2, v24
	v_fmac_f32_e32 v39, v3, v11
	v_fmac_f32_e32 v38, v3, v25
	v_fmac_f32_e32 v39, v4, v12
	v_fmac_f32_e32 v38, v4, v26
	v_fmac_f32_e32 v39, v5, v13
	v_fmac_f32_e32 v38, v5, v27
	v_fmac_f32_e32 v39, v6, v14
	v_fmac_f32_e32 v38, v6, v28
	v_fmac_f32_e32 v39, v7, v15
	v_fmac_f32_e32 v38, v7, v29
	v_fmac_f32_e32 v39, v8, v16
	v_fmac_f32_e32 v38, v8, v30
	v_fmac_f32_e32 v39, v9, v17
	v_fmac_f32_e32 v38, v9, v31
	v_add_u32_e32 v18, 0x3200, v42
	v_add_u32_e32 v22, 0x3200, v41
	ds_read_b128 v[2:5], v0 offset:128
	ds_read_b128 v[6:9], v0 offset:144
	ds_read2_b32 v[10:11], v18 offset1:100
	ds_read2_b32 v[24:25], v22 offset1:100
	v_add_u32_e32 v19, 0x200, v18
	v_add_u32_e32 v23, 0x200, v22
	ds_read2_b32 v[12:13], v19 offset0:72 offset1:172
	ds_read2_b32 v[26:27], v23 offset0:72 offset1:172
	v_add_u32_e32 v20, 0x400, v18
	v_add_u32_e32 v32, 0x400, v22
	ds_read2_b32 v[14:15], v20 offset0:144 offset1:244
	ds_read2_b32 v[28:29], v32 offset0:144 offset1:244
	v_add_u32_e32 v21, 0x800, v18
	v_add_u32_e32 v33, 0x800, v22
	ds_read2_b32 v[16:17], v21 offset0:88 offset1:188
	ds_read2_b32 v[30:31], v33 offset0:88 offset1:188
	s_waitcnt lgkmcnt(10)
	v_fmac_f32_e32 v39, v46, v54
	v_fmac_f32_e32 v38, v46, v62
	v_fmac_f32_e32 v39, v47, v55
	v_fmac_f32_e32 v38, v47, v63
	v_fmac_f32_e32 v39, v48, v56
	v_fmac_f32_e32 v38, v48, v64
	v_fmac_f32_e32 v39, v49, v57
	v_fmac_f32_e32 v38, v49, v65
	v_fmac_f32_e32 v39, v50, v58
	v_fmac_f32_e32 v38, v50, v66
	v_fmac_f32_e32 v39, v51, v59
	v_fmac_f32_e32 v38, v51, v67
	v_fmac_f32_e32 v39, v52, v60
	v_fmac_f32_e32 v38, v52, v68
	v_fmac_f32_e32 v39, v53, v61
	v_fmac_f32_e32 v38, v53, v69
	v_add_u32_e32 v70, 0x3e80, v42
	v_add_u32_e32 v74, 0x3e80, v41
	ds_read_b128 v[46:49], v0 offset:160
	ds_read_b128 v[50:53], v0 offset:176
	ds_read2_b32 v[54:55], v70 offset1:100
	ds_read2_b32 v[62:63], v74 offset1:100
	v_add_u32_e32 v71, 0x200, v70
	v_add_u32_e32 v75, 0x200, v74
	ds_read2_b32 v[56:57], v71 offset0:72 offset1:172
	ds_read2_b32 v[64:65], v75 offset0:72 offset1:172
	v_add_u32_e32 v72, 0x400, v70
	v_add_u32_e32 v76, 0x400, v74
	ds_read2_b32 v[58:59], v72 offset0:144 offset1:244
	ds_read2_b32 v[66:67], v76 offset0:144 offset1:244
	v_add_u32_e32 v73, 0x800, v70
	v_add_u32_e32 v77, 0x800, v74
	ds_read2_b32 v[60:61], v73 offset0:88 offset1:188
	ds_read2_b32 v[68:69], v77 offset0:88 offset1:188
	s_waitcnt lgkmcnt(10)
	v_fmac_f32_e32 v39, v2, v10
	v_fmac_f32_e32 v38, v2, v24
	v_fmac_f32_e32 v39, v3, v11
	v_fmac_f32_e32 v38, v3, v25
	v_fmac_f32_e32 v39, v4, v12
	v_fmac_f32_e32 v38, v4, v26
	v_fmac_f32_e32 v39, v5, v13
	v_fmac_f32_e32 v38, v5, v27
	v_fmac_f32_e32 v39, v6, v14
	v_fmac_f32_e32 v38, v6, v28
	v_fmac_f32_e32 v39, v7, v15
	v_fmac_f32_e32 v38, v7, v29
	v_fmac_f32_e32 v39, v8, v16
	v_fmac_f32_e32 v38, v8, v30
	v_fmac_f32_e32 v39, v9, v17
	v_fmac_f32_e32 v38, v9, v31
	v_add_u32_e32 v18, 0x4b00, v42
	v_add_u32_e32 v22, 0x4b00, v41
	ds_read_b128 v[2:5], v0 offset:192
	ds_read_b128 v[6:9], v0 offset:208
	ds_read2_b32 v[10:11], v18 offset1:100
	ds_read2_b32 v[24:25], v22 offset1:100
	v_add_u32_e32 v19, 0x200, v18
	v_add_u32_e32 v23, 0x200, v22
	ds_read2_b32 v[12:13], v19 offset0:72 offset1:172
	ds_read2_b32 v[26:27], v23 offset0:72 offset1:172
	v_add_u32_e32 v20, 0x400, v18
	v_add_u32_e32 v32, 0x400, v22
	ds_read2_b32 v[14:15], v20 offset0:144 offset1:244
	ds_read2_b32 v[28:29], v32 offset0:144 offset1:244
	v_add_u32_e32 v21, 0x800, v18
	v_add_u32_e32 v33, 0x800, v22
	ds_read2_b32 v[16:17], v21 offset0:88 offset1:188
	ds_read2_b32 v[30:31], v33 offset0:88 offset1:188
	s_waitcnt lgkmcnt(10)
	v_fmac_f32_e32 v39, v46, v54
	v_fmac_f32_e32 v38, v46, v62
	v_fmac_f32_e32 v39, v47, v55
	v_fmac_f32_e32 v38, v47, v63
	v_fmac_f32_e32 v39, v48, v56
	v_fmac_f32_e32 v38, v48, v64
	v_fmac_f32_e32 v39, v49, v57
	v_fmac_f32_e32 v38, v49, v65
	v_fmac_f32_e32 v39, v50, v58
	v_fmac_f32_e32 v38, v50, v66
	v_fmac_f32_e32 v39, v51, v59
	v_fmac_f32_e32 v38, v51, v67
	v_fmac_f32_e32 v39, v52, v60
	v_fmac_f32_e32 v38, v52, v68
	v_fmac_f32_e32 v39, v53, v61
	v_fmac_f32_e32 v38, v53, v69
	v_add_u32_e32 v70, 0x5780, v42
	v_add_u32_e32 v74, 0x5780, v41
	ds_read_b128 v[46:49], v0 offset:224
	ds_read_b128 v[50:53], v0 offset:240
	ds_read2_b32 v[54:55], v70 offset1:100
	ds_read2_b32 v[62:63], v74 offset1:100
	v_add_u32_e32 v71, 0x200, v70
	v_add_u32_e32 v75, 0x200, v74
	ds_read2_b32 v[56:57], v71 offset0:72 offset1:172
	ds_read2_b32 v[64:65], v75 offset0:72 offset1:172
	v_add_u32_e32 v72, 0x400, v70
	v_add_u32_e32 v76, 0x400, v74
	ds_read2_b32 v[58:59], v72 offset0:144 offset1:244
	ds_read2_b32 v[66:67], v76 offset0:144 offset1:244
	v_add_u32_e32 v73, 0x800, v70
	v_add_u32_e32 v77, 0x800, v74
	ds_read2_b32 v[60:61], v73 offset0:88 offset1:188
	ds_read2_b32 v[68:69], v77 offset0:88 offset1:188
	s_waitcnt lgkmcnt(10)
	v_fmac_f32_e32 v39, v2, v10
	v_fmac_f32_e32 v38, v2, v24
	v_fmac_f32_e32 v39, v3, v11
	v_fmac_f32_e32 v38, v3, v25
	v_fmac_f32_e32 v39, v4, v12
	v_fmac_f32_e32 v38, v4, v26
	v_fmac_f32_e32 v39, v5, v13
	v_fmac_f32_e32 v38, v5, v27
	v_fmac_f32_e32 v39, v6, v14
	v_fmac_f32_e32 v38, v6, v28
	v_fmac_f32_e32 v39, v7, v15
	v_fmac_f32_e32 v38, v7, v29
	v_fmac_f32_e32 v39, v8, v16
	v_fmac_f32_e32 v38, v8, v30
	v_fmac_f32_e32 v39, v9, v17
	v_fmac_f32_e32 v38, v9, v31
	s_waitcnt lgkmcnt(0)
	v_fmac_f32_e32 v39, v46, v54
	v_fmac_f32_e32 v38, v46, v62
	v_fmac_f32_e32 v39, v47, v55
	v_fmac_f32_e32 v38, v47, v63
	v_fmac_f32_e32 v39, v48, v56
	v_fmac_f32_e32 v38, v48, v64
	v_fmac_f32_e32 v39, v49, v57
	v_fmac_f32_e32 v38, v49, v65
	v_fmac_f32_e32 v39, v50, v58
	v_fmac_f32_e32 v38, v50, v66
	v_fmac_f32_e32 v39, v51, v59
	v_fmac_f32_e32 v38, v51, v67
	v_fmac_f32_e32 v39, v52, v60
	v_fmac_f32_e32 v38, v52, v68
	v_fmac_f32_e32 v39, v53, v61
	v_fmac_f32_e32 v38, v53, v69
	v_cmp_nlt_f32_e64 s[0:1], 0, v39
	s_and_saveexec_b64 s[2:3], s[0:1]
	s_cbranch_execz .LBB4_55
	v_mul_f32_e32 v0, 0x3fb8aa3b, v39
	v_rndne_f32_e32 v0, v0
	v_fmamk_f32 v1, v0, 0xbf317218, v39
	v_fmamk_f32 v1, v0, 0x3102e308, v1
	v_mov_b32_e32 v2, 0x3ab69700
	v_fmac_f32_e32 v2, 0x395133b1, v1
	v_fmaak_f32 v2, v1, v2, 0x3c0887f9
	v_fmaak_f32 v2, v1, v2, 0x3d2aaa81
	v_cvt_i32_f32_e32 v3, v0
	v_fmaak_f32 v2, v1, v2, 0x3e2aaaab
	v_fma_f32 v2, v1, v2, 0.5
	v_mul_f32_e32 v2, v1, v2
	s_mov_b32 s0, 0x43000000
	v_fmac_f32_e32 v1, v1, v2
	v_ldexp_f32 v2, 1.0, v3
	v_mov_b32_e32 v3, 0x7f000000
	v_cmp_eq_f32_e64 s[0:1], s0, v0
	s_nop 1
	v_cndmask_b32_e64 v0, v2, v3, s[0:1]
	v_add_f32_e32 v2, -1.0, v0
	v_fmac_f32_e32 v2, v0, v1
	v_add_f32_e32 v0, v2, v2
	v_cndmask_b32_e64 v0, v2, v0, s[0:1]
	s_mov_b32 s0, 0xc1880000
	v_cmp_ngt_f32_e64 s[0:1], s0, v39
	s_nop 1
	v_cndmask_b32_e64 v39, -1.0, v0, s[0:1]
